# routing top-8 threshold search stops once exactly 8 keys are selected; stacked on tile-ordered e, barrier early invalidate, rowpass hoists
# speedup vs baseline: 1.0383x; 1.0073x over previous
; __device__ __forceinline__ float sigmoidf_(float x) { return __builtin_amdgcn_rcpf(1.f + __expf(-x)); }
; __device__ __forceinline__ void phase_route(const Ptrs& P, LAS unsigned char* lds, int layer, int tid_, int vcu, int G) {
;     ...
;             const float s0 = sigmoidf_(nl0), s1 = sigmoidf_(nl1);
;             if (i < 7) { nl0 = lg[(size_t)(t + 1) * 128 + lane]; nl1 = lg[(size_t)(t + 1) * 128 + 64 + lane]; }
;             const float v0 = s0 + rb0, v1 = s1 + rb1;
;             unsigned k0 = __float_as_uint(v0), k1 = __float_as_uint(v1);
;             k0 = (k0 & 0x80000000u) ? ~k0 : (k0 | 0x80000000u); k1 = (k1 & 0x80000000u) ? ~k1 : (k1 | 0x80000000u);
;             k0 = (k0 & ~127u) | (unsigned)(127 - lane); k1 = (k1 & ~127u) | (unsigned)(63 - lane);
;             unsigned thr = 0u;
; #pragma unroll
;             for (int b = 31; b >= 0; --b) { const unsigned cand = thr | (1u << b);
;                 const int c = __popcll(__ballot(k0 >= cand)) + __popcll(__ballot(k1 >= cand));
;                 if (c >= 8) thr = cand; }
.LBB0_1130:
	v_mul_f32_e32 v18, 0xbfb8aa3b, v18
	v_mul_f32_e32 v17, 0xbfb8aa3b, v17
	v_exp_f32_e32 v18, v18
	v_exp_f32_e32 v17, v17
	v_add_f32_e32 v18, 1.0, v18
	v_add_f32_e32 v17, 1.0, v17
	v_rcp_f32_e32 v19, v18
	v_rcp_f32_e32 v18, v17
	s_nop 0
	v_pk_add_f32 v[30:31], v[6:7], v[18:19]
	s_nop 0
	v_and_b32_e32 v33, 0x7fffffff, v31
	v_and_b32_e32 v32, 0x7fffffff, v30
	v_xor_b32_e32 v17, -1, v31
	v_pk_add_f32 v[32:33], v[32:33], 0 neg_lo:[1,1] neg_hi:[1,1]
	v_cmp_gt_i32_e32 vcc, 0, v31
	v_xor_b32_e32 v29, -1, v30
	s_nop 0
	v_cndmask_b32_e32 v17, v33, v17, vcc
	v_cmp_gt_i32_e32 vcc, 0, v30
	v_and_b32_e32 v30, 0xffffff80, v17
	v_or_b32_e32 v30, v30, v3
	v_cndmask_b32_e32 v29, v32, v29, vcc
	v_cmp_gt_i32_e32 vcc, 0, v17
	s_bcnt1_i32_b64 s6, vcc
	v_cmp_gt_i32_e32 vcc, 0, v29
	s_bcnt1_i32_b64 s7, vcc
	s_add_i32 s7, s7, s6
	s_cmp_gt_u32 s7, 7
	v_and_b32_e32 v31, 0xffffff80, v29
	s_cselect_b32 s6, 0x80000000, 0
	v_or_b32_e32 v31, v31, v4
	v_xor_b32_e32 v30, 0x7f, v30
	s_or_b32 s7, s6, 2.0
	v_xor_b32_e32 v31, 63, v31
	v_cmp_le_u32_e32 vcc, s7, v30
	s_bcnt1_i32_b64 s8, vcc
	v_cmp_le_u32_e32 vcc, s7, v31
	s_bcnt1_i32_b64 s9, vcc
	s_add_i32 s9, s9, s8
	s_cmp_gt_u32 s9, 7
	s_cselect_b32 s6, s7, s6
	s_cmp_eq_u32 s9, 8
	s_cbranch_scc1 .Lroute_thr_found
	s_or_b32 s7, s6, 0x20000000
	v_cmp_le_u32_e32 vcc, s7, v30
	s_bcnt1_i32_b64 s8, vcc
	v_cmp_le_u32_e32 vcc, s7, v31
	s_bcnt1_i32_b64 s9, vcc
	s_add_i32 s9, s9, s8
	s_cmp_gt_u32 s9, 7
	s_cselect_b32 s6, s7, s6
	s_cmp_eq_u32 s9, 8
	s_cbranch_scc1 .Lroute_thr_found
	s_or_b32 s7, s6, 0x10000000
	v_cmp_le_u32_e32 vcc, s7, v30
	s_bcnt1_i32_b64 s8, vcc
	v_cmp_le_u32_e32 vcc, s7, v31
	s_bcnt1_i32_b64 s9, vcc
	s_add_i32 s9, s9, s8
	s_cmp_gt_u32 s9, 7
	s_cselect_b32 s6, s7, s6
	s_cmp_eq_u32 s9, 8
	s_cbranch_scc1 .Lroute_thr_found
	s_or_b32 s7, s6, 0x8000000
	v_cmp_le_u32_e32 vcc, s7, v30
	s_bcnt1_i32_b64 s8, vcc
	v_cmp_le_u32_e32 vcc, s7, v31
	s_bcnt1_i32_b64 s9, vcc
	s_add_i32 s9, s9, s8
	s_cmp_gt_u32 s9, 7
	s_cselect_b32 s6, s7, s6
	s_cmp_eq_u32 s9, 8
	s_cbranch_scc1 .Lroute_thr_found
	s_or_b32 s7, s6, 0x4000000
	v_cmp_le_u32_e32 vcc, s7, v30
	s_bcnt1_i32_b64 s8, vcc
	v_cmp_le_u32_e32 vcc, s7, v31
	s_bcnt1_i32_b64 s9, vcc
	s_add_i32 s9, s9, s8
	s_cmp_gt_u32 s9, 7
	s_cselect_b32 s6, s7, s6
	s_cmp_eq_u32 s9, 8
	s_cbranch_scc1 .Lroute_thr_found
	s_or_b32 s7, s6, 0x2000000
	v_cmp_le_u32_e32 vcc, s7, v30
	s_bcnt1_i32_b64 s8, vcc
	v_cmp_le_u32_e32 vcc, s7, v31
	s_bcnt1_i32_b64 s9, vcc
	s_add_i32 s9, s9, s8
	s_cmp_gt_u32 s9, 7
	s_cselect_b32 s6, s7, s6
	s_cmp_eq_u32 s9, 8
	s_cbranch_scc1 .Lroute_thr_found
	s_or_b32 s7, s6, 0x1000000
	v_cmp_le_u32_e32 vcc, s7, v30
	s_bcnt1_i32_b64 s8, vcc
	v_cmp_le_u32_e32 vcc, s7, v31
	s_bcnt1_i32_b64 s9, vcc
	s_add_i32 s9, s9, s8
	s_cmp_gt_u32 s9, 7
	s_cselect_b32 s6, s7, s6
	s_cmp_eq_u32 s9, 8
	s_cbranch_scc1 .Lroute_thr_found
	s_or_b32 s7, s6, 0x800000
	v_cmp_le_u32_e32 vcc, s7, v30
	s_bcnt1_i32_b64 s8, vcc
	v_cmp_le_u32_e32 vcc, s7, v31
	s_bcnt1_i32_b64 s9, vcc
	s_add_i32 s9, s9, s8
	s_cmp_gt_u32 s9, 7
	s_cselect_b32 s6, s7, s6
	s_cmp_eq_u32 s9, 8
	s_cbranch_scc1 .Lroute_thr_found
	s_or_b32 s7, s6, 0x400000
	v_cmp_le_u32_e32 vcc, s7, v30
	s_bcnt1_i32_b64 s8, vcc
	v_cmp_le_u32_e32 vcc, s7, v31
	s_bcnt1_i32_b64 s9, vcc
	s_add_i32 s9, s9, s8
	s_cmp_gt_u32 s9, 7
	s_cselect_b32 s6, s7, s6
	s_cmp_eq_u32 s9, 8
	s_cbranch_scc1 .Lroute_thr_found
	s_or_b32 s7, s6, 0x200000
	v_cmp_le_u32_e32 vcc, s7, v30
	s_bcnt1_i32_b64 s8, vcc
	v_cmp_le_u32_e32 vcc, s7, v31
	s_bcnt1_i32_b64 s9, vcc
	s_add_i32 s9, s9, s8
	s_cmp_gt_u32 s9, 7
	s_cselect_b32 s6, s7, s6
	s_cmp_eq_u32 s9, 8
	s_cbranch_scc1 .Lroute_thr_found
	s_or_b32 s7, s6, 0x100000
	v_cmp_le_u32_e32 vcc, s7, v30
	s_bcnt1_i32_b64 s8, vcc
	v_cmp_le_u32_e32 vcc, s7, v31
	s_bcnt1_i32_b64 s9, vcc
	s_add_i32 s9, s9, s8
	s_cmp_gt_u32 s9, 7
	s_cselect_b32 s6, s7, s6
	s_cmp_eq_u32 s9, 8
	s_cbranch_scc1 .Lroute_thr_found
	s_or_b32 s7, s6, 0x80000
	v_cmp_le_u32_e32 vcc, s7, v30
	s_bcnt1_i32_b64 s8, vcc
	v_cmp_le_u32_e32 vcc, s7, v31
	s_bcnt1_i32_b64 s9, vcc
	s_add_i32 s9, s9, s8
	s_cmp_gt_u32 s9, 7
	s_cselect_b32 s6, s7, s6
	s_cmp_eq_u32 s9, 8
	s_cbranch_scc1 .Lroute_thr_found
	s_or_b32 s7, s6, 0x40000
	v_cmp_le_u32_e32 vcc, s7, v30
	s_bcnt1_i32_b64 s8, vcc
	v_cmp_le_u32_e32 vcc, s7, v31
	s_bcnt1_i32_b64 s9, vcc
	s_add_i32 s9, s9, s8
	s_cmp_gt_u32 s9, 7
	s_cselect_b32 s6, s7, s6
	s_cmp_eq_u32 s9, 8
	s_cbranch_scc1 .Lroute_thr_found
	s_or_b32 s7, s6, 0x20000
	v_cmp_le_u32_e32 vcc, s7, v30
	s_bcnt1_i32_b64 s8, vcc
	v_cmp_le_u32_e32 vcc, s7, v31
	s_bcnt1_i32_b64 s9, vcc
	s_add_i32 s9, s9, s8
	s_cmp_gt_u32 s9, 7
	s_cselect_b32 s6, s7, s6
	s_cmp_eq_u32 s9, 8
	s_cbranch_scc1 .Lroute_thr_found
; __device__ __forceinline__ void phase_route(const Ptrs& P, LAS unsigned char* lds, int layer, int tid_, int vcu, int G) {
;     ...
;             for (int b = 31; b >= 0; --b) { const unsigned cand = thr | (1u << b);
;                 const int c = __popcll(__ballot(k0 >= cand)) + __popcll(__ballot(k1 >= cand));
;                 if (c >= 8) thr = cand; }
;             const bool sel0 = k0 >= thr, sel1 = k1 >= thr;
;             const unsigned long long m0 = __ballot(sel0), m1 = __ballot(sel1), below = (1ull << lane) - 1ull;
;             const int r0 = __popcll(m0 & below), r1 = __popcll(m0) + __popcll(m1 & below);
;             const int lp0 = (wave * 8 + i) * 8;
;             if (sel0) { ssel[r0] = s0; pe[lp0 + r0] = lane; prank[lp0 + r0] = __hip_atomic_fetch_add(hist + lane, 1, __ATOMIC_RELAXED, __HIP_MEMORY_SCOPE_WORKGROUP); }
;             if (sel1) { ssel[r1] = s1; pe[lp0 + r1] = lane + 64; prank[lp0 + r1] = __hip_atomic_fetch_add(hist + lane + 64, 1, __ATOMIC_RELAXED, __HIP_MEMORY_SCOPE_WORKGROUP); }
	s_or_b32 s7, s6, 0x10000
	v_cmp_le_u32_e32 vcc, s7, v30
	s_bcnt1_i32_b64 s8, vcc
	v_cmp_le_u32_e32 vcc, s7, v31
	s_bcnt1_i32_b64 s9, vcc
	s_add_i32 s9, s9, s8
	s_cmp_gt_u32 s9, 7
	s_cselect_b32 s6, s7, s6
	s_cmp_eq_u32 s9, 8
	s_cbranch_scc1 .Lroute_thr_found
	s_or_b32 s7, s6, 0x8000
	v_cmp_le_u32_e32 vcc, s7, v30
	s_bcnt1_i32_b64 s8, vcc
	v_cmp_le_u32_e32 vcc, s7, v31
	s_bcnt1_i32_b64 s9, vcc
	s_add_i32 s9, s9, s8
	s_cmp_gt_u32 s9, 7
	s_cselect_b32 s6, s7, s6
	s_cmp_eq_u32 s9, 8
	s_cbranch_scc1 .Lroute_thr_found
	s_or_b32 s7, s6, 0x4000
	v_cmp_le_u32_e32 vcc, s7, v30
	s_bcnt1_i32_b64 s8, vcc
	v_cmp_le_u32_e32 vcc, s7, v31
	s_bcnt1_i32_b64 s9, vcc
	s_add_i32 s9, s9, s8
	s_cmp_gt_u32 s9, 7
	s_cselect_b32 s6, s7, s6
	s_cmp_eq_u32 s9, 8
	s_cbranch_scc1 .Lroute_thr_found
	s_or_b32 s7, s6, 0x2000
	v_cmp_le_u32_e32 vcc, s7, v30
	s_bcnt1_i32_b64 s8, vcc
	v_cmp_le_u32_e32 vcc, s7, v31
	s_bcnt1_i32_b64 s9, vcc
	s_add_i32 s9, s9, s8
	s_cmp_gt_u32 s9, 7
	s_cselect_b32 s6, s7, s6
	s_cmp_eq_u32 s9, 8
	s_cbranch_scc1 .Lroute_thr_found
	s_or_b32 s7, s6, 0x1000
	v_cmp_le_u32_e32 vcc, s7, v30
	s_bcnt1_i32_b64 s8, vcc
	v_cmp_le_u32_e32 vcc, s7, v31
	s_bcnt1_i32_b64 s9, vcc
	s_add_i32 s9, s9, s8
	s_cmp_gt_u32 s9, 7
	s_cselect_b32 s6, s7, s6
	s_cmp_eq_u32 s9, 8
	s_cbranch_scc1 .Lroute_thr_found
	s_or_b32 s7, s6, 0x800
	v_cmp_le_u32_e32 vcc, s7, v30
	s_bcnt1_i32_b64 s8, vcc
	v_cmp_le_u32_e32 vcc, s7, v31
	s_bcnt1_i32_b64 s9, vcc
	s_add_i32 s9, s9, s8
	s_cmp_gt_u32 s9, 7
	s_cselect_b32 s6, s7, s6
	s_cmp_eq_u32 s9, 8
	s_cbranch_scc1 .Lroute_thr_found
	s_or_b32 s7, s6, 0x400
	v_cmp_le_u32_e32 vcc, s7, v30
	s_bcnt1_i32_b64 s8, vcc
	v_cmp_le_u32_e32 vcc, s7, v31
	s_bcnt1_i32_b64 s9, vcc
	s_add_i32 s9, s9, s8
	s_cmp_gt_u32 s9, 7
	s_cselect_b32 s6, s7, s6
	s_cmp_eq_u32 s9, 8
	s_cbranch_scc1 .Lroute_thr_found
	s_or_b32 s7, s6, 0x200
	v_cmp_le_u32_e32 vcc, s7, v30
	s_bcnt1_i32_b64 s8, vcc
	v_cmp_le_u32_e32 vcc, s7, v31
	s_bcnt1_i32_b64 s9, vcc
	s_add_i32 s9, s9, s8
	s_cmp_gt_u32 s9, 7
	s_cselect_b32 s6, s7, s6
	s_cmp_eq_u32 s9, 8
	s_cbranch_scc1 .Lroute_thr_found
	s_or_b32 s7, s6, 0x100
	v_cmp_le_u32_e32 vcc, s7, v30
	s_bcnt1_i32_b64 s8, vcc
	v_cmp_le_u32_e32 vcc, s7, v31
	s_bcnt1_i32_b64 s9, vcc
	s_add_i32 s9, s9, s8
	s_cmp_gt_u32 s9, 7
	s_cselect_b32 s6, s7, s6
	s_cmp_eq_u32 s9, 8
	s_cbranch_scc1 .Lroute_thr_found
	s_or_b32 s7, s6, 0x80
	v_cmp_le_u32_e32 vcc, s7, v30
	s_bcnt1_i32_b64 s8, vcc
	v_cmp_le_u32_e32 vcc, s7, v31
	s_bcnt1_i32_b64 s9, vcc
	s_add_i32 s9, s9, s8
	s_cmp_gt_u32 s9, 7
	s_cselect_b32 s6, s7, s6
	s_cmp_eq_u32 s9, 8
	s_cbranch_scc1 .Lroute_thr_found
	s_or_b32 s7, s6, 64
	v_cmp_le_u32_e32 vcc, s7, v30
	s_bcnt1_i32_b64 s8, vcc
	v_cmp_le_u32_e32 vcc, s7, v31
	s_bcnt1_i32_b64 s9, vcc
	s_add_i32 s9, s9, s8
	s_cmp_gt_u32 s9, 7
	s_cselect_b32 s6, s7, s6
	s_cmp_eq_u32 s9, 8
	s_cbranch_scc1 .Lroute_thr_found
	s_or_b32 s7, s6, 32
	v_cmp_le_u32_e32 vcc, s7, v30
	s_bcnt1_i32_b64 s8, vcc
	v_cmp_le_u32_e32 vcc, s7, v31
	s_bcnt1_i32_b64 s9, vcc
	s_add_i32 s9, s9, s8
	s_cmp_gt_u32 s9, 7
	s_cselect_b32 s6, s7, s6
	s_cmp_eq_u32 s9, 8
	s_cbranch_scc1 .Lroute_thr_found
	s_or_b32 s7, s6, 16
	v_cmp_le_u32_e32 vcc, s7, v30
	s_bcnt1_i32_b64 s8, vcc
	v_cmp_le_u32_e32 vcc, s7, v31
	s_bcnt1_i32_b64 s9, vcc
	s_add_i32 s9, s9, s8
	s_cmp_gt_u32 s9, 7
	s_cselect_b32 s6, s7, s6
	s_cmp_eq_u32 s9, 8
	s_cbranch_scc1 .Lroute_thr_found
	s_or_b32 s7, s6, 8
	v_cmp_le_u32_e32 vcc, s7, v30
	s_bcnt1_i32_b64 s8, vcc
	v_cmp_le_u32_e32 vcc, s7, v31
	s_bcnt1_i32_b64 s9, vcc
	s_add_i32 s9, s9, s8
	s_cmp_gt_u32 s9, 7
	s_cselect_b32 s6, s7, s6
	s_cmp_eq_u32 s9, 8
	s_cbranch_scc1 .Lroute_thr_found
	s_or_b32 s7, s6, 4
	v_cmp_le_u32_e32 vcc, s7, v30
	s_bcnt1_i32_b64 s8, vcc
	v_cmp_le_u32_e32 vcc, s7, v31
	s_bcnt1_i32_b64 s9, vcc
	s_add_i32 s9, s9, s8
	s_cmp_gt_u32 s9, 7
	s_cselect_b32 s6, s7, s6
	s_cmp_eq_u32 s9, 8
	s_cbranch_scc1 .Lroute_thr_found
	s_or_b32 s7, s6, 2
	v_cmp_le_u32_e32 vcc, s7, v30
	s_bcnt1_i32_b64 s8, vcc
	v_cmp_le_u32_e32 vcc, s7, v31
	s_bcnt1_i32_b64 s9, vcc
	s_add_i32 s9, s9, s8
	s_cmp_gt_u32 s9, 7
	s_cselect_b32 s6, s7, s6
	s_cmp_eq_u32 s9, 8
	s_cbranch_scc1 .Lroute_thr_found
	s_or_b32 s7, s6, 1
	v_cmp_le_u32_e32 vcc, s7, v30
	s_bcnt1_i32_b64 s8, vcc
	v_cmp_le_u32_e32 vcc, s7, v31
	s_bcnt1_i32_b64 s9, vcc
	s_add_i32 s9, s9, s8
	s_cmp_gt_u32 s9, 7
	s_cselect_b32 s6, s7, s6
.Lroute_thr_found:
	v_cmp_le_u32_e64 s[42:43], s6, v30
	v_cmp_le_u32_e32 vcc, s6, v31
	s_and_saveexec_b64 s[6:7], s[42:43]
	s_cbranch_execz .LBB0_1132
	v_and_b32_e32 v29, s42, v10
	v_and_b32_e32 v17, s43, v1
	v_bcnt_u32_b32 v29, v29, 0
	v_bcnt_u32_b32 v17, v17, v29
	v_lshl_add_u32 v29, v17, 2, v21
	v_add3_u32 v17, v24, s5, v17
	v_lshl_add_u32 v17, v17, 2, 0
	ds_write_b32 v29, v19 offset:12288
	ds_write_b32 v17, v4 offset:1024
	ds_add_rtn_u32 v19, v22, v197
	s_waitcnt lgkmcnt(0)
	ds_write_b32 v17, v19 offset:3072
